# finish loop: next-row prefetch kept in flight (ladder recounted, cur<-next copies moved to iteration end)
# speedup vs baseline: 1.0190x; 1.0078x over previous
.LBB0_710:
	v_and_b32_e32 v221, 0xffff0000, v180
	v_mul_f32_e32 v222, 0xbfb8aa3b, v221
	v_exp_f32_e32 v222, v222
	v_lshlrev_b32_e32 v220, 16, v180
	v_and_b32_e32 v223, 0xffff0000, v181
	v_mul_f32_e32 v180, 0xbfb8aa3b, v220
	v_add_f32_e32 v224, 1.0, v222
	v_lshlrev_b32_e32 v222, 16, v181
	v_mul_f32_e32 v181, 0xbfb8aa3b, v222
	v_exp_f32_e32 v225, v181
	v_mul_f32_e32 v181, 0xbfb8aa3b, v223
	v_exp_f32_e32 v180, v180
	v_exp_f32_e32 v226, v181
	v_rcp_f32_e32 v181, v224
	v_add_f32_e32 v224, 1.0, v225
	v_add_f32_e32 v180, 1.0, v180
	v_add_f32_e32 v225, 1.0, v226
	v_rcp_f32_e32 v180, v180
	v_rcp_f32_e32 v224, v224
	v_rcp_f32_e32 v225, v225
	v_lshlrev_b32_e32 v226, 16, v164
	v_and_b32_e32 v227, 0xffff0000, v164
	v_mul_f32_e32 v164, 0x3d372713, v226
	v_pk_mul_f32 v[180:181], v[180:181], v[220:221]
	v_pk_mul_f32 v[220:221], v[224:225], v[222:223]
	v_lshlrev_b32_e32 v224, 16, v168
	v_and_b32_e32 v225, 0xffff0000, v168
	v_mul_f32_e32 v164, v164, v226
	v_mov_b32_e32 v168, v226
	v_fmac_f32_e32 v168, v164, v168
	v_mul_f32_e32 v164, 0x3f4c422a, v168
	v_mul_f32_e32 v168, 0x3d372713, v227
	v_mul_f32_e32 v168, v168, v227
	v_mov_b32_e32 v228, v227
	v_fmac_f32_e32 v228, v168, v228
	v_add_f32_e32 v164, v164, v164
	v_mul_f32_e32 v168, 0x3f4c422a, v228
	v_mul_f32_e32 v164, 0x3fb8aa3b, v164
	v_add_f32_e32 v168, v168, v168
	v_exp_f32_e32 v164, v164
	v_mul_f32_e32 v168, 0x3fb8aa3b, v168
	v_exp_f32_e32 v229, v168
	v_lshlrev_b32_e32 v222, 16, v176
	v_and_b32_e32 v223, 0xffff0000, v176
	v_lshlrev_b32_e32 v176, 16, v177
	v_and_b32_e32 v177, 0xffff0000, v177
	v_lshlrev_b32_e32 v168, 16, v169
	v_add_f32_e32 v164, 1.0, v164
	v_and_b32_e32 v169, 0xffff0000, v169
	v_rcp_f32_e32 v228, v164
	v_add_f32_e32 v164, 1.0, v229
	v_pk_add_f32 v[176:177], v[168:169], v[176:177]
	v_pk_add_f32 v[168:169], v[224:225], v[222:223]
	v_pk_mul_f32 v[224:225], v[226:227], 0.5 op_sel_hi:[1,0]
	v_lshlrev_b32_e32 v226, 16, v165
	v_rcp_f32_e32 v229, v164
	v_mul_f32_e32 v164, 0x3d372713, v226
	v_and_b32_e32 v227, 0xffff0000, v165
	v_mul_f32_e32 v164, v164, v226
	v_mov_b32_e32 v165, v226
	v_fmac_f32_e32 v165, v164, v165
	v_mul_f32_e32 v164, 0x3f4c422a, v165
	v_add_f32_e32 v164, v164, v164
	v_mul_f32_e32 v164, 0x3fb8aa3b, v164
	v_pk_fma_f32 v[222:223], v[228:229], 2.0, 1.0 op_sel_hi:[1,0,0] neg_lo:[1,0,0] neg_hi:[1,0,0]
	v_exp_f32_e32 v228, v164
	v_mul_f32_e32 v164, 0x3d372713, v227
	v_mul_f32_e32 v164, v164, v227
	v_mov_b32_e32 v165, v227
	v_fmac_f32_e32 v165, v164, v165
	v_mul_f32_e32 v164, 0x3f4c422a, v165
	v_add_f32_e32 v164, v164, v164
	v_mul_f32_e32 v164, 0x3fb8aa3b, v164
	v_exp_f32_e32 v229, v164
	v_pk_add_f32 v[164:165], v[222:223], 1.0 op_sel_hi:[1,0]
	v_add_f32_e32 v222, 1.0, v228
	v_rcp_f32_e32 v222, v222
	v_add_f32_e32 v223, 1.0, v229
	v_rcp_f32_e32 v223, v223
	v_pk_mul_f32 v[164:165], v[224:225], v[164:165]
	v_pk_add_f32 v[202:203], v[202:203], v[204:205]
	v_pk_mul_f32 v[164:165], v[168:169], v[164:165]
	v_pk_fma_f32 v[168:169], v[222:223], 2.0, 1.0 op_sel_hi:[1,0,0] neg_lo:[1,0,0] neg_hi:[1,0,0]
	v_cvt_pk_bf16_f32 v164, v164, v165
	v_pk_add_f32 v[224:225], v[168:169], 1.0 op_sel_hi:[1,0]
	v_mov_b64_e32 v[168:169], s[12:13]
	v_pk_fma_f32 v[202:203], v[202:203], s[10:11], v[168:169] op_sel_hi:[1,0,0]
	v_pk_mul_f32 v[222:223], v[226:227], 0.5 op_sel_hi:[1,0]
	v_mul_f32_e32 v165, 0x4b800000, v203
	v_cmp_gt_f32_e32 vcc, s7, v203
	v_pk_mul_f32 v[204:205], v[222:223], v[224:225]
	s_nop 0
	v_cndmask_b32_e32 v165, v203, v165, vcc
	v_rsq_f32_e32 v203, v165
	v_pk_mul_f32 v[176:177], v[176:177], v[204:205]
	s_nop 0
	v_cvt_pk_bf16_f32 v165, v176, v177
	v_mul_f32_e32 v176, 0x45800000, v203
	v_cndmask_b32_e32 v176, v203, v176, vcc
	v_pk_mul_f32 v[196:197], v[196:197], v[176:177] op_sel_hi:[1,0]
	v_pk_mul_f32 v[176:177], v[194:195], v[176:177] op_sel_hi:[1,0]
	s_waitcnt vmcnt(43)
	v_pk_mul_f32 v[28:29], v[28:29], v[196:197]
	v_pk_mul_f32 v[30:31], v[30:31], v[176:177]
	v_pk_mul_f32 v[28:29], v[180:181], v[28:29]
	v_pk_mul_f32 v[30:31], v[220:221], v[30:31]
	v_cvt_pk_bf16_f32 v28, v28, v29
	v_cvt_pk_bf16_f32 v29, v30, v31
	v_mul_f32_e32 v30, 0x4b800000, v202
	v_cmp_gt_f32_e32 vcc, s7, v202
	v_and_b32_e32 v31, 0xffff0000, v154
	v_mul_f32_e32 v176, 0xbfb8aa3b, v31
	v_cndmask_b32_e32 v30, v202, v30, vcc
	v_rsq_f32_e32 v180, v30
	v_lshlrev_b32_e32 v30, 16, v154
	v_mul_f32_e32 v154, 0xbfb8aa3b, v30
	v_exp_f32_e32 v154, v154
	v_exp_f32_e32 v177, v176
	v_mul_f32_e32 v181, 0x45800000, v180
	v_add_f32_e32 v154, 1.0, v154
	v_rcp_f32_e32 v176, v154
	v_add_f32_e32 v154, 1.0, v177
	v_rcp_f32_e32 v177, v154
	v_cndmask_b32_e32 v154, v180, v181, vcc
	v_pk_mul_f32 v[180:181], v[192:193], v[154:155] op_sel_hi:[1,0]
	v_pk_mul_f32 v[30:31], v[176:177], v[30:31]
	v_lshlrev_b32_e32 v176, 16, v155
	v_mul_f32_e32 v177, 0xbfb8aa3b, v176
	s_waitcnt vmcnt(41)
	v_pk_mul_f32 v[24:25], v[24:25], v[180:181]
	v_exp_f32_e32 v180, v177
	v_and_b32_e32 v177, 0xffff0000, v155
	v_pk_mul_f32 v[24:25], v[30:31], v[24:25]
	v_mul_f32_e32 v30, 0xbfb8aa3b, v177
	v_exp_f32_e32 v31, v30
	v_cvt_pk_bf16_f32 v24, v24, v25
	v_add_f32_e32 v25, 1.0, v180
	v_pk_mul_f32 v[154:155], v[190:191], v[154:155] op_sel_hi:[1,0]
	v_rcp_f32_e32 v30, v25
	v_pk_mul_f32 v[26:27], v[26:27], v[154:155]
	v_add_f32_e32 v25, 1.0, v31
	v_lshlrev_b32_e32 v154, 16, v150
	v_rcp_f32_e32 v31, v25
	v_and_b32_e32 v155, 0xffff0000, v150
	v_mul_f32_e32 v25, 0xbfb8aa3b, v154
	v_exp_f32_e32 v25, v25
	v_mul_f32_e32 v150, 0xbfb8aa3b, v155
	v_exp_f32_e32 v180, v150
	v_pk_mul_f32 v[30:31], v[30:31], v[176:177]
	v_lshlrev_b32_e32 v176, 16, v151
	v_add_f32_e32 v25, 1.0, v25
	v_and_b32_e32 v177, 0xffff0000, v151
	v_mul_f32_e32 v151, 0xbfb8aa3b, v176
	v_rcp_f32_e32 v150, v25
	v_add_f32_e32 v25, 1.0, v180
	v_exp_f32_e32 v180, v151
	v_mul_f32_e32 v151, 0xbfb8aa3b, v177
	v_exp_f32_e32 v181, v151
	v_rcp_f32_e32 v151, v25
	v_add_f32_e32 v25, 1.0, v180
	v_rcp_f32_e32 v180, v25
	v_add_f32_e32 v25, 1.0, v181
	v_rcp_f32_e32 v181, v25
	v_pk_mul_f32 v[26:27], v[30:31], v[26:27]
	v_pk_mul_f32 v[30:31], v[150:151], v[154:155]
	v_lshlrev_b32_e32 v154, 16, v146
	v_pk_mul_f32 v[150:151], v[180:181], v[176:177]
	v_lshlrev_b32_e32 v176, 16, v144
	v_and_b32_e32 v177, 0xffff0000, v144
	v_mul_f32_e32 v144, 0x3d372713, v176
	v_and_b32_e32 v155, 0xffff0000, v146
	v_mul_f32_e32 v144, v144, v176
	v_mov_b32_e32 v146, v176
	v_fmac_f32_e32 v146, v144, v146
	v_mul_f32_e32 v144, 0x3f4c422a, v146
	v_mul_f32_e32 v146, 0x3d372713, v177
	v_mul_f32_e32 v146, v146, v177
	v_mov_b32_e32 v180, v177
	v_fmac_f32_e32 v180, v146, v180
	v_add_f32_e32 v144, v144, v144
	v_mul_f32_e32 v146, 0x3f4c422a, v180
	v_mul_f32_e32 v144, 0x3fb8aa3b, v144
	v_add_f32_e32 v146, v146, v146
	v_exp_f32_e32 v144, v144
	v_mul_f32_e32 v146, 0x3fb8aa3b, v146
	v_exp_f32_e32 v181, v146
	v_cvt_pk_bf16_f32 v25, v26, v27
	v_add_f32_e32 v144, 1.0, v144
	v_rcp_f32_e32 v180, v144
	v_add_f32_e32 v144, 1.0, v181
	v_lshlrev_b32_e32 v26, 16, v148
	v_and_b32_e32 v27, 0xffff0000, v148
	v_rcp_f32_e32 v181, v144
	v_lshlrev_b32_e32 v144, 16, v145
	v_pk_add_f32 v[26:27], v[154:155], v[26:27]
	v_pk_mul_f32 v[154:155], v[176:177], 0.5 op_sel_hi:[1,0]
	v_mul_f32_e32 v176, 0x3d372713, v144
	v_mul_f32_e32 v176, v176, v144
	v_mov_b32_e32 v177, v144
	v_and_b32_e32 v145, 0xffff0000, v145
	v_fmac_f32_e32 v177, v176, v177
	v_lshlrev_b32_e32 v148, 16, v149
	v_and_b32_e32 v149, 0xffff0000, v149
	v_lshlrev_b32_e32 v146, 16, v147
	v_and_b32_e32 v147, 0xffff0000, v147
	v_mul_f32_e32 v176, 0x3f4c422a, v177
	v_mul_f32_e32 v177, 0x3d372713, v145
	v_pk_add_f32 v[146:147], v[146:147], v[148:149]
	v_pk_fma_f32 v[148:149], v[180:181], 2.0, 1.0 op_sel_hi:[1,0,0] neg_lo:[1,0,0] neg_hi:[1,0,0]
	v_mul_f32_e32 v177, v177, v145
	v_mov_b32_e32 v180, v145
	v_fmac_f32_e32 v180, v177, v180
	v_mul_f32_e32 v177, 0x3f4c422a, v180
	v_add_f32_e32 v176, v176, v176
	v_add_f32_e32 v177, v177, v177
	v_mul_f32_e32 v176, 0x3fb8aa3b, v176
	v_mul_f32_e32 v177, 0x3fb8aa3b, v177
	v_exp_f32_e32 v176, v176
	v_exp_f32_e32 v177, v177
	v_pk_add_f32 v[148:149], v[148:149], 1.0 op_sel_hi:[1,0]
	v_pk_mul_f32 v[144:145], v[144:145], 0.5 op_sel_hi:[1,0]
	v_add_f32_e32 v176, 1.0, v176
	v_add_f32_e32 v177, 1.0, v177
	v_rcp_f32_e32 v176, v176
	v_rcp_f32_e32 v177, v177
	v_pk_mul_f32 v[148:149], v[154:155], v[148:149]
	s_waitcnt lgkmcnt(4)
	v_pk_add_f32 v[154:155], v[206:207], v[208:209]
	v_pk_mul_f32 v[26:27], v[26:27], v[148:149]
	v_pk_fma_f32 v[154:155], v[154:155], s[10:11], v[168:169] op_sel_hi:[1,0,0]
	v_cvt_pk_bf16_f32 v26, v26, v27
	v_mul_f32_e32 v27, 0x4b800000, v155
	v_cmp_gt_f32_e32 vcc, s7, v155
	v_pk_fma_f32 v[148:149], v[176:177], 2.0, 1.0 op_sel_hi:[1,0,0] neg_lo:[1,0,0] neg_hi:[1,0,0]
	v_cndmask_b32_e32 v27, v155, v27, vcc
	v_rsq_f32_e32 v155, v27
	v_pk_add_f32 v[148:149], v[148:149], 1.0 op_sel_hi:[1,0]
	v_pk_mul_f32 v[144:145], v[144:145], v[148:149]
	v_pk_mul_f32 v[144:145], v[146:147], v[144:145]
	s_nop 0
	v_cvt_pk_bf16_f32 v27, v144, v145
	v_mul_f32_e32 v144, 0x45800000, v155
	v_cndmask_b32_e32 v144, v155, v144, vcc
	v_pk_mul_f32 v[146:147], v[188:189], v[144:145] op_sel_hi:[1,0]
	v_cmp_gt_f32_e32 vcc, s7, v154
	v_pk_mul_f32 v[20:21], v[20:21], v[146:147]
	v_pk_mul_f32 v[20:21], v[30:31], v[20:21]
	v_pk_mul_f32 v[30:31], v[186:187], v[144:145] op_sel_hi:[1,0]
	v_cvt_pk_bf16_f32 v20, v20, v21
	v_pk_mul_f32 v[22:23], v[22:23], v[30:31]
	s_nop 0
	v_pk_mul_f32 v[22:23], v[150:151], v[22:23]
	v_cvt_pk_bf16_f32 v21, v22, v23
	v_mul_f32_e32 v22, 0x4b800000, v154
	v_cndmask_b32_e32 v22, v154, v22, vcc
	v_rsq_f32_e32 v144, v22
	v_lshlrev_b32_e32 v22, 16, v142
	v_and_b32_e32 v23, 0xffff0000, v142
	v_mul_f32_e32 v30, 0xbfb8aa3b, v22
	v_mul_f32_e32 v31, 0xbfb8aa3b, v23
	v_exp_f32_e32 v30, v30
	v_exp_f32_e32 v31, v31
	v_mul_f32_e32 v142, 0x45800000, v144
	v_cndmask_b32_e32 v142, v144, v142, vcc
	v_add_f32_e32 v30, 1.0, v30
	v_add_f32_e32 v31, 1.0, v31
	v_rcp_f32_e32 v30, v30
	v_rcp_f32_e32 v31, v31
	v_pk_mul_f32 v[144:145], v[178:179], v[142:143] op_sel_hi:[1,0]
	s_waitcnt vmcnt(40)
	v_pk_mul_f32 v[16:17], v[16:17], v[144:145]
	v_pk_mul_f32 v[22:23], v[30:31], v[22:23]
	v_lshlrev_b32_e32 v30, 16, v143
	v_mul_f32_e32 v31, 0xbfb8aa3b, v30
	v_exp_f32_e32 v144, v31
	v_and_b32_e32 v31, 0xffff0000, v143
	v_pk_mul_f32 v[16:17], v[22:23], v[16:17]
	v_mul_f32_e32 v22, 0xbfb8aa3b, v31
	v_exp_f32_e32 v23, v22
	v_cvt_pk_bf16_f32 v16, v16, v17
	v_add_f32_e32 v17, 1.0, v144
	v_pk_mul_f32 v[142:143], v[170:171], v[142:143] op_sel_hi:[1,0]
	v_rcp_f32_e32 v22, v17
	v_pk_mul_f32 v[18:19], v[18:19], v[142:143]
	v_add_f32_e32 v17, 1.0, v23
	v_lshlrev_b32_e32 v142, 16, v140
	v_rcp_f32_e32 v23, v17
	v_and_b32_e32 v143, 0xffff0000, v140
	v_mul_f32_e32 v17, 0xbfb8aa3b, v142
	v_exp_f32_e32 v17, v17
	v_mul_f32_e32 v140, 0xbfb8aa3b, v143
	v_exp_f32_e32 v140, v140
	v_pk_mul_f32 v[22:23], v[22:23], v[30:31]
	v_add_f32_e32 v17, 1.0, v17
	v_rcp_f32_e32 v30, v17
	v_add_f32_e32 v17, 1.0, v140
	v_lshlrev_b32_e32 v140, 16, v141
	v_and_b32_e32 v141, 0xffff0000, v141
	v_mul_f32_e32 v31, 0xbfb8aa3b, v140
	v_exp_f32_e32 v144, v31
	v_mul_f32_e32 v31, 0xbfb8aa3b, v141
	v_exp_f32_e32 v145, v31
	v_rcp_f32_e32 v31, v17
	v_add_f32_e32 v17, 1.0, v144
	v_rcp_f32_e32 v144, v17
	v_add_f32_e32 v17, 1.0, v145
	v_rcp_f32_e32 v145, v17
	v_pk_mul_f32 v[18:19], v[22:23], v[18:19]
	v_pk_mul_f32 v[22:23], v[30:31], v[142:143]
	v_lshlrev_b32_e32 v142, 16, v134
	v_and_b32_e32 v143, 0xffff0000, v134
	v_mul_f32_e32 v134, 0x3d372713, v142
	v_pk_mul_f32 v[30:31], v[144:145], v[140:141]
	v_lshlrev_b32_e32 v140, 16, v136
	v_and_b32_e32 v141, 0xffff0000, v136
	v_mul_f32_e32 v134, v134, v142
	v_mov_b32_e32 v136, v142
	v_fmac_f32_e32 v136, v134, v136
	v_mul_f32_e32 v134, 0x3f4c422a, v136
	v_mul_f32_e32 v136, 0x3d372713, v143
	v_mul_f32_e32 v136, v136, v143
	v_mov_b32_e32 v144, v143
	v_fmac_f32_e32 v144, v136, v144
	v_add_f32_e32 v134, v134, v134
	v_mul_f32_e32 v136, 0x3f4c422a, v144
	v_mul_f32_e32 v134, 0x3fb8aa3b, v134
	v_add_f32_e32 v136, v136, v136
	v_exp_f32_e32 v134, v134
	v_mul_f32_e32 v136, 0x3fb8aa3b, v136
	v_exp_f32_e32 v145, v136
	v_cvt_pk_bf16_f32 v17, v18, v19
	v_add_f32_e32 v134, 1.0, v134
	v_rcp_f32_e32 v144, v134
	v_add_f32_e32 v134, 1.0, v145
	v_lshlrev_b32_e32 v18, 16, v138
	v_and_b32_e32 v19, 0xffff0000, v138
	v_rcp_f32_e32 v145, v134
	v_lshlrev_b32_e32 v134, 16, v135
	v_pk_add_f32 v[18:19], v[140:141], v[18:19]
	v_pk_mul_f32 v[140:141], v[142:143], 0.5 op_sel_hi:[1,0]
	v_mul_f32_e32 v142, 0x3d372713, v134
	v_mul_f32_e32 v142, v142, v134
	v_mov_b32_e32 v143, v134
	v_and_b32_e32 v135, 0xffff0000, v135
	v_fmac_f32_e32 v143, v142, v143
	v_lshlrev_b32_e32 v138, 16, v139
	v_and_b32_e32 v139, 0xffff0000, v139
	v_lshlrev_b32_e32 v136, 16, v137
	v_and_b32_e32 v137, 0xffff0000, v137
	v_mul_f32_e32 v142, 0x3f4c422a, v143
	v_mul_f32_e32 v143, 0x3d372713, v135
	v_pk_add_f32 v[136:137], v[136:137], v[138:139]
	v_pk_fma_f32 v[138:139], v[144:145], 2.0, 1.0 op_sel_hi:[1,0,0] neg_lo:[1,0,0] neg_hi:[1,0,0]
	v_mul_f32_e32 v143, v143, v135
	v_mov_b32_e32 v144, v135
	v_fmac_f32_e32 v144, v143, v144
	v_mul_f32_e32 v143, 0x3f4c422a, v144
	v_add_f32_e32 v142, v142, v142
	v_add_f32_e32 v143, v143, v143
	v_mul_f32_e32 v142, 0x3fb8aa3b, v142
	v_mul_f32_e32 v143, 0x3fb8aa3b, v143
	v_exp_f32_e32 v142, v142
	v_exp_f32_e32 v143, v143
	v_pk_add_f32 v[138:139], v[138:139], 1.0 op_sel_hi:[1,0]
	v_pk_mul_f32 v[134:135], v[134:135], 0.5 op_sel_hi:[1,0]
	v_add_f32_e32 v142, 1.0, v142
	v_add_f32_e32 v143, 1.0, v143
	v_rcp_f32_e32 v142, v142
	v_rcp_f32_e32 v143, v143
	v_pk_mul_f32 v[138:139], v[140:141], v[138:139]
	s_waitcnt lgkmcnt(2)
	v_pk_add_f32 v[140:141], v[198:199], v[200:201]
	v_pk_mul_f32 v[18:19], v[18:19], v[138:139]
	v_pk_fma_f32 v[140:141], v[140:141], s[10:11], v[168:169] op_sel_hi:[1,0,0]
	v_cvt_pk_bf16_f32 v18, v18, v19
	v_mul_f32_e32 v19, 0x4b800000, v141
	v_cmp_gt_f32_e32 vcc, s7, v141
	v_pk_fma_f32 v[138:139], v[142:143], 2.0, 1.0 op_sel_hi:[1,0,0] neg_lo:[1,0,0] neg_hi:[1,0,0]
	v_cndmask_b32_e32 v19, v141, v19, vcc
	v_rsq_f32_e32 v141, v19
	v_pk_add_f32 v[138:139], v[138:139], 1.0 op_sel_hi:[1,0]
	v_pk_mul_f32 v[134:135], v[134:135], v[138:139]
	v_pk_mul_f32 v[134:135], v[136:137], v[134:135]
	s_nop 0
	v_cvt_pk_bf16_f32 v19, v134, v135
	v_mul_f32_e32 v134, 0x45800000, v141
	v_cndmask_b32_e32 v134, v141, v134, vcc
	v_pk_mul_f32 v[136:137], v[174:175], v[134:135] op_sel_hi:[1,0]
	v_cmp_gt_f32_e32 vcc, s7, v140
	s_waitcnt vmcnt(39)
	v_pk_mul_f32 v[12:13], v[12:13], v[136:137]
	v_pk_mul_f32 v[12:13], v[22:23], v[12:13]
	v_pk_mul_f32 v[22:23], v[172:173], v[134:135] op_sel_hi:[1,0]
	v_cvt_pk_bf16_f32 v12, v12, v13
	v_pk_mul_f32 v[14:15], v[14:15], v[22:23]
	s_nop 0
	v_pk_mul_f32 v[14:15], v[30:31], v[14:15]
	s_nop 0
	v_cvt_pk_bf16_f32 v13, v14, v15
	v_mul_f32_e32 v14, 0x4b800000, v140
	v_cndmask_b32_e32 v14, v140, v14, vcc
	v_rsq_f32_e32 v30, v14
	v_lshlrev_b32_e32 v14, 16, v132
	v_and_b32_e32 v15, 0xffff0000, v132
	v_mul_f32_e32 v22, 0xbfb8aa3b, v14
	v_mul_f32_e32 v23, 0xbfb8aa3b, v15
	v_exp_f32_e32 v22, v22
	v_exp_f32_e32 v23, v23
	v_mul_f32_e32 v31, 0x45800000, v30
	v_cndmask_b32_e32 v30, v30, v31, vcc
	v_add_f32_e32 v22, 1.0, v22
	v_add_f32_e32 v23, 1.0, v23
	v_rcp_f32_e32 v22, v22
	v_rcp_f32_e32 v23, v23
	v_pk_mul_f32 v[134:135], v[160:161], v[30:31] op_sel_hi:[1,0]
	s_waitcnt vmcnt(37)
	v_pk_mul_f32 v[8:9], v[8:9], v[134:135]
	v_pk_mul_f32 v[14:15], v[22:23], v[14:15]
	v_lshlrev_b32_e32 v22, 16, v133
	v_mul_f32_e32 v23, 0xbfb8aa3b, v22
	v_exp_f32_e32 v31, v23
	v_and_b32_e32 v23, 0xffff0000, v133
	v_pk_mul_f32 v[8:9], v[14:15], v[8:9]
	v_mul_f32_e32 v14, 0xbfb8aa3b, v23
	v_exp_f32_e32 v15, v14
	v_cvt_pk_bf16_f32 v8, v8, v9
	v_add_f32_e32 v9, 1.0, v31
	v_pk_mul_f32 v[30:31], v[158:159], v[30:31] op_sel_hi:[1,0]
	v_rcp_f32_e32 v14, v9
	v_pk_mul_f32 v[10:11], v[10:11], v[30:31]
	v_add_f32_e32 v9, 1.0, v15
	v_lshlrev_b32_e32 v30, 16, v130
	v_rcp_f32_e32 v15, v9
	v_and_b32_e32 v31, 0xffff0000, v130
	v_mul_f32_e32 v9, 0xbfb8aa3b, v30
	v_exp_f32_e32 v9, v9
	v_mul_f32_e32 v130, 0xbfb8aa3b, v31
	v_exp_f32_e32 v130, v130
	v_pk_mul_f32 v[14:15], v[14:15], v[22:23]
	v_add_f32_e32 v9, 1.0, v9
	v_rcp_f32_e32 v22, v9
	v_add_f32_e32 v9, 1.0, v130
	v_lshlrev_b32_e32 v130, 16, v131
	v_and_b32_e32 v131, 0xffff0000, v131
	v_mul_f32_e32 v23, 0xbfb8aa3b, v130
	v_exp_f32_e32 v132, v23
	v_mul_f32_e32 v23, 0xbfb8aa3b, v131
	v_exp_f32_e32 v133, v23
	v_rcp_f32_e32 v23, v9
	v_add_f32_e32 v9, 1.0, v132
	v_rcp_f32_e32 v132, v9
	v_add_f32_e32 v9, 1.0, v133
	v_rcp_f32_e32 v133, v9
	v_pk_mul_f32 v[10:11], v[14:15], v[10:11]
	v_cvt_pk_bf16_f32 v9, v10, v11
	v_pk_mul_f32 v[14:15], v[132:133], v[130:131]
	v_lshlrev_b32_e32 v130, 16, v120
	v_and_b32_e32 v131, 0xffff0000, v120
	v_mul_f32_e32 v120, 0x3d372713, v130
	v_pk_mul_f32 v[10:11], v[22:23], v[30:31]
	v_lshlrev_b32_e32 v22, 16, v128
	v_and_b32_e32 v23, 0xffff0000, v128
	v_lshlrev_b32_e32 v30, 16, v129
	v_and_b32_e32 v31, 0xffff0000, v129
	v_lshlrev_b32_e32 v128, 16, v126
	v_and_b32_e32 v129, 0xffff0000, v126
	v_mul_f32_e32 v120, v120, v130
	v_mov_b32_e32 v126, v130
	v_fmac_f32_e32 v126, v120, v126
	v_mul_f32_e32 v120, 0x3f4c422a, v126
	v_mul_f32_e32 v126, 0x3d372713, v131
	v_mul_f32_e32 v126, v126, v131
	v_mov_b32_e32 v132, v131
	v_fmac_f32_e32 v132, v126, v132
	v_add_f32_e32 v120, v120, v120
	v_mul_f32_e32 v126, 0x3f4c422a, v132
	v_mul_f32_e32 v120, 0x3fb8aa3b, v120
	v_add_f32_e32 v126, v126, v126
	v_exp_f32_e32 v120, v120
	v_mul_f32_e32 v126, 0x3fb8aa3b, v126
	v_exp_f32_e32 v133, v126
	v_pk_add_f32 v[22:23], v[22:23], v[128:129]
	v_add_f32_e32 v120, 1.0, v120
	v_rcp_f32_e32 v132, v120
	v_add_f32_e32 v120, 1.0, v133
	v_rcp_f32_e32 v133, v120
	v_lshlrev_b32_e32 v120, 16, v121
	v_pk_mul_f32 v[128:129], v[130:131], 0.5 op_sel_hi:[1,0]
	v_mul_f32_e32 v130, 0x3d372713, v120
	v_mul_f32_e32 v130, v130, v120
	v_mov_b32_e32 v131, v120
	v_and_b32_e32 v121, 0xffff0000, v121
	v_fmac_f32_e32 v131, v130, v131
	v_lshlrev_b32_e32 v126, 16, v127
	v_and_b32_e32 v127, 0xffff0000, v127
	v_mul_f32_e32 v130, 0x3f4c422a, v131
	v_mul_f32_e32 v131, 0x3d372713, v121
	v_pk_add_f32 v[30:31], v[30:31], v[126:127]
	v_pk_fma_f32 v[126:127], v[132:133], 2.0, 1.0 op_sel_hi:[1,0,0] neg_lo:[1,0,0] neg_hi:[1,0,0]
	v_mul_f32_e32 v131, v131, v121
	v_mov_b32_e32 v132, v121
	v_fmac_f32_e32 v132, v131, v132
	v_mul_f32_e32 v131, 0x3f4c422a, v132
	v_add_f32_e32 v130, v130, v130
	v_add_f32_e32 v131, v131, v131
	v_mul_f32_e32 v130, 0x3fb8aa3b, v130
	v_mul_f32_e32 v131, 0x3fb8aa3b, v131
	v_exp_f32_e32 v130, v130
	v_exp_f32_e32 v131, v131
	v_pk_add_f32 v[126:127], v[126:127], 1.0 op_sel_hi:[1,0]
	v_pk_mul_f32 v[120:121], v[120:121], 0.5 op_sel_hi:[1,0]
	v_add_f32_e32 v130, 1.0, v130
	v_add_f32_e32 v131, 1.0, v131
	v_rcp_f32_e32 v130, v130
	v_rcp_f32_e32 v131, v131
	v_pk_mul_f32 v[126:127], v[128:129], v[126:127]
	s_waitcnt lgkmcnt(0)
	v_pk_add_f32 v[128:129], v[182:183], v[184:185]
	v_pk_mul_f32 v[22:23], v[22:23], v[126:127]
	v_pk_fma_f32 v[128:129], v[128:129], s[10:11], v[168:169] op_sel_hi:[1,0,0]
	v_cvt_pk_bf16_f32 v22, v22, v23
	v_mul_f32_e32 v23, 0x4b800000, v129
	v_cmp_gt_f32_e32 vcc, s7, v129
	v_pk_fma_f32 v[126:127], v[130:131], 2.0, 1.0 op_sel_hi:[1,0,0] neg_lo:[1,0,0] neg_hi:[1,0,0]
	v_cndmask_b32_e32 v23, v129, v23, vcc
	v_rsq_f32_e32 v129, v23
	v_pk_add_f32 v[126:127], v[126:127], 1.0 op_sel_hi:[1,0]
	v_pk_mul_f32 v[120:121], v[120:121], v[126:127]
	v_pk_mul_f32 v[30:31], v[30:31], v[120:121]
	v_cvt_pk_bf16_f32 v23, v30, v31
	v_mul_f32_e32 v30, 0x45800000, v129
	v_cndmask_b32_e32 v30, v129, v30, vcc
	v_pk_mul_f32 v[120:121], v[166:167], v[30:31] op_sel_hi:[1,0]
	v_cmp_gt_f32_e32 vcc, s7, v128
	v_pk_mul_f32 v[0:1], v[0:1], v[120:121]
	v_pk_mul_f32 v[0:1], v[10:11], v[0:1]
	v_pk_mul_f32 v[10:11], v[162:163], v[30:31] op_sel_hi:[1,0]
	v_cvt_pk_bf16_f32 v0, v0, v1
	v_pk_mul_f32 v[2:3], v[2:3], v[10:11]
	s_nop 0
	v_pk_mul_f32 v[2:3], v[14:15], v[2:3]
	s_nop 0
	v_cvt_pk_bf16_f32 v1, v2, v3
	v_mul_f32_e32 v2, 0x4b800000, v128
	v_cndmask_b32_e32 v2, v128, v2, vcc
	v_rsq_f32_e32 v14, v2
	v_lshlrev_b32_e32 v2, 16, v82
	v_and_b32_e32 v3, 0xffff0000, v82
	v_mul_f32_e32 v10, 0xbfb8aa3b, v2
	v_mul_f32_e32 v11, 0xbfb8aa3b, v3
	v_exp_f32_e32 v10, v10
	v_exp_f32_e32 v11, v11
	v_mul_f32_e32 v15, 0x45800000, v14
	v_cndmask_b32_e32 v14, v14, v15, vcc
	v_add_f32_e32 v10, 1.0, v10
	v_add_f32_e32 v11, 1.0, v11
	v_rcp_f32_e32 v10, v10
	v_rcp_f32_e32 v11, v11
	v_pk_mul_f32 v[30:31], v[156:157], v[14:15] op_sel_hi:[1,0]
	s_waitcnt vmcnt(36)
	v_pk_mul_f32 v[4:5], v[4:5], v[30:31]
	v_pk_mul_f32 v[2:3], v[10:11], v[2:3]
	v_lshlrev_b32_e32 v10, 16, v83
	v_and_b32_e32 v11, 0xffff0000, v83
	v_mul_f32_e32 v15, 0xbfb8aa3b, v10
	v_mul_f32_e32 v30, 0xbfb8aa3b, v11
	v_exp_f32_e32 v15, v15
	v_exp_f32_e32 v30, v30
	v_pk_mul_f32 v[2:3], v[2:3], v[4:5]
	v_add_f32_e32 v4, 1.0, v15
	v_add_f32_e32 v5, 1.0, v30
	v_rcp_f32_e32 v4, v4
	v_rcp_f32_e32 v5, v5
	v_pk_mul_f32 v[14:15], v[152:153], v[14:15] op_sel_hi:[1,0]
	v_cvt_pk_bf16_f32 v2, v2, v3
	v_pk_mul_f32 v[6:7], v[6:7], v[14:15]
	v_pk_mul_f32 v[4:5], v[4:5], v[10:11]
	s_nop 0
	v_pk_mul_f32 v[4:5], v[4:5], v[6:7]
	s_nop 0
	v_cvt_pk_bf16_f32 v3, v4, v5
	v_add_co_u32_e32 v4, vcc, s11, v64
	s_nop 1
	v_addc_co_u32_e32 v5, vcc, -1, v65, vcc
	v_add_co_u32_e32 v6, vcc, s13, v64
	global_store_dwordx2 v[4:5], v[28:29], off offset:-1536
	s_nop 0
	v_addc_co_u32_e32 v7, vcc, -1, v65, vcc
	global_store_dwordx2 v[6:7], v[164:165], off offset:-1536
	global_store_dwordx2 v[64:65], v[24:25], off offset:-1536
	global_store_dwordx2 v[4:5], v[20:21], off offset:-1024
	global_store_dwordx2 v[6:7], v[26:27], off offset:-1024
	global_store_dwordx2 v[64:65], v[16:17], off offset:-1024
	global_store_dwordx2 v[4:5], v[12:13], off offset:-512
	global_store_dwordx2 v[6:7], v[18:19], off offset:-512
	global_store_dwordx2 v[64:65], v[8:9], off offset:-512
	global_store_dwordx2 v[4:5], v[0:1], off
	global_store_dwordx2 v[6:7], v[22:23], off
	global_store_dwordx2 v[64:65], v[2:3], off
	v_lshl_add_u64 v[64:65], v[64:65], 0, s[8:9]
	s_andn2_b64 vcc, exec, s[14:15]
	s_waitcnt vmcnt(12)
	v_mov_b64_e32 v[176:177], v[88:89]
	v_mov_b64_e32 v[180:181], v[90:91]
	v_mov_b64_e32 v[148:149], v[104:105]
	v_mov_b64_e32 v[146:147], v[108:109]
	v_mov_b64_e32 v[150:151], v[112:113]
	v_mov_b64_e32 v[154:155], v[86:87]
	v_mov_b64_e32 v[142:143], v[94:95]
	v_mov_b64_e32 v[144:145], v[92:93]
	v_mov_b64_e32 v[138:139], v[100:101]
	v_mov_b64_e32 v[136:137], v[102:103]
	v_mov_b64_e32 v[140:141], v[98:99]
	v_mov_b64_e32 v[134:135], v[96:97]
	v_mov_b64_e32 v[168:169], v[106:107]
	v_mov_b64_e32 v[132:133], v[116:117]
	v_mov_b64_e32 v[130:131], v[118:119]
	v_mov_b64_e32 v[126:127], v[114:115]
	v_mov_b64_e32 v[120:121], v[122:123]
	v_mov_b64_e32 v[128:129], v[110:111]
	v_mov_b64_e32 v[82:83], v[124:125]
	v_mov_b64_e32 v[164:165], v[84:85]
	s_cbranch_vccz .LBB0_713

.Lfin_nopf_0:
	s_waitcnt vmcnt(0)
	s_branch .LBB0_710

.LBB0_2534:
	v_and_b32_e32 v233, 0xffff0000, v190
	v_mul_f32_e32 v234, 0xbfb8aa3b, v233
	v_exp_f32_e32 v234, v234
	v_lshlrev_b32_e32 v232, 16, v190
	v_and_b32_e32 v235, 0xffff0000, v191
	v_mul_f32_e32 v190, 0xbfb8aa3b, v232
	v_add_f32_e32 v236, 1.0, v234
	v_lshlrev_b32_e32 v234, 16, v191
	v_mul_f32_e32 v191, 0xbfb8aa3b, v234
	v_exp_f32_e32 v237, v191
	v_mul_f32_e32 v191, 0xbfb8aa3b, v235
	v_exp_f32_e32 v190, v190
	v_exp_f32_e32 v238, v191
	v_rcp_f32_e32 v191, v236
	v_add_f32_e32 v236, 1.0, v237
	v_add_f32_e32 v190, 1.0, v190
	v_add_f32_e32 v237, 1.0, v238
	v_rcp_f32_e32 v190, v190
	v_rcp_f32_e32 v236, v236
	v_rcp_f32_e32 v237, v237
	v_lshlrev_b32_e32 v238, 16, v174
	v_and_b32_e32 v239, 0xffff0000, v174
	v_mul_f32_e32 v174, 0x3d372713, v238
	v_pk_mul_f32 v[190:191], v[190:191], v[232:233]
	v_pk_mul_f32 v[232:233], v[236:237], v[234:235]
	v_lshlrev_b32_e32 v236, 16, v176
	v_and_b32_e32 v237, 0xffff0000, v176
	v_mul_f32_e32 v174, v174, v238
	v_mov_b32_e32 v176, v238
	v_fmac_f32_e32 v176, v174, v176
	v_mul_f32_e32 v174, 0x3f4c422a, v176
	v_mul_f32_e32 v176, 0x3d372713, v239
	v_mul_f32_e32 v176, v176, v239
	v_mov_b32_e32 v240, v239
	v_fmac_f32_e32 v240, v176, v240
	v_add_f32_e32 v174, v174, v174
	v_mul_f32_e32 v176, 0x3f4c422a, v240
	v_mul_f32_e32 v174, 0x3fb8aa3b, v174
	v_add_f32_e32 v176, v176, v176
	v_exp_f32_e32 v174, v174
	v_mul_f32_e32 v176, 0x3fb8aa3b, v176
	v_exp_f32_e32 v241, v176
	v_lshlrev_b32_e32 v234, 16, v184
	v_and_b32_e32 v235, 0xffff0000, v184
	v_lshlrev_b32_e32 v184, 16, v185
	v_and_b32_e32 v185, 0xffff0000, v185
	v_lshlrev_b32_e32 v176, 16, v177
	v_add_f32_e32 v174, 1.0, v174
	v_and_b32_e32 v177, 0xffff0000, v177
	v_rcp_f32_e32 v240, v174
	v_add_f32_e32 v174, 1.0, v241
	v_pk_add_f32 v[184:185], v[176:177], v[184:185]
	v_pk_add_f32 v[176:177], v[236:237], v[234:235]
	v_pk_mul_f32 v[236:237], v[238:239], 0.5 op_sel_hi:[1,0]
	v_lshlrev_b32_e32 v238, 16, v175
	v_rcp_f32_e32 v241, v174
	v_mul_f32_e32 v174, 0x3d372713, v238
	v_and_b32_e32 v239, 0xffff0000, v175
	v_mul_f32_e32 v174, v174, v238
	v_mov_b32_e32 v175, v238
	v_fmac_f32_e32 v175, v174, v175
	v_mul_f32_e32 v174, 0x3f4c422a, v175
	v_add_f32_e32 v174, v174, v174
	v_mul_f32_e32 v174, 0x3fb8aa3b, v174
	v_pk_fma_f32 v[234:235], v[240:241], 2.0, 1.0 op_sel_hi:[1,0,0] neg_lo:[1,0,0] neg_hi:[1,0,0]
	v_exp_f32_e32 v240, v174
	v_mul_f32_e32 v174, 0x3d372713, v239
	v_mul_f32_e32 v174, v174, v239
	v_mov_b32_e32 v175, v239
	v_fmac_f32_e32 v175, v174, v175
	v_mul_f32_e32 v174, 0x3f4c422a, v175
	v_add_f32_e32 v174, v174, v174
	v_mul_f32_e32 v174, 0x3fb8aa3b, v174
	v_exp_f32_e32 v241, v174
	v_pk_add_f32 v[174:175], v[234:235], 1.0 op_sel_hi:[1,0]
	v_add_f32_e32 v234, 1.0, v240
	v_rcp_f32_e32 v234, v234
	v_add_f32_e32 v235, 1.0, v241
	v_rcp_f32_e32 v235, v235
	v_pk_mul_f32 v[174:175], v[236:237], v[174:175]
	v_pk_add_f32 v[214:215], v[214:215], v[216:217]
	v_pk_mul_f32 v[174:175], v[176:177], v[174:175]
	v_pk_fma_f32 v[176:177], v[234:235], 2.0, 1.0 op_sel_hi:[1,0,0] neg_lo:[1,0,0] neg_hi:[1,0,0]
	v_cvt_pk_bf16_f32 v174, v174, v175
	v_pk_add_f32 v[236:237], v[176:177], 1.0 op_sel_hi:[1,0]
	v_mov_b64_e32 v[176:177], s[12:13]
	v_pk_fma_f32 v[214:215], v[214:215], s[10:11], v[176:177] op_sel_hi:[1,0,0]
	v_pk_mul_f32 v[234:235], v[238:239], 0.5 op_sel_hi:[1,0]
	v_mul_f32_e32 v175, 0x4b800000, v215
	v_cmp_gt_f32_e32 vcc, s7, v215
	v_pk_mul_f32 v[216:217], v[234:235], v[236:237]
	s_nop 0
	v_cndmask_b32_e32 v175, v215, v175, vcc
	v_rsq_f32_e32 v215, v175
	v_pk_mul_f32 v[184:185], v[184:185], v[216:217]
	s_nop 0
	v_cvt_pk_bf16_f32 v175, v184, v185
	v_mul_f32_e32 v184, 0x45800000, v215
	v_cndmask_b32_e32 v184, v215, v184, vcc
	v_pk_mul_f32 v[208:209], v[208:209], v[184:185] op_sel_hi:[1,0]
	v_pk_mul_f32 v[184:185], v[206:207], v[184:185] op_sel_hi:[1,0]
	s_waitcnt vmcnt(43)
	v_pk_mul_f32 v[24:25], v[24:25], v[208:209]
	v_pk_mul_f32 v[26:27], v[26:27], v[184:185]
	v_pk_mul_f32 v[24:25], v[190:191], v[24:25]
	v_pk_mul_f32 v[26:27], v[232:233], v[26:27]
	v_cvt_pk_bf16_f32 v24, v24, v25
	v_cvt_pk_bf16_f32 v25, v26, v27
	v_mul_f32_e32 v26, 0x4b800000, v214
	v_cmp_gt_f32_e32 vcc, s7, v214
	v_and_b32_e32 v27, 0xffff0000, v168
	v_mul_f32_e32 v184, 0xbfb8aa3b, v27
	v_cndmask_b32_e32 v26, v214, v26, vcc
	v_rsq_f32_e32 v190, v26
	v_lshlrev_b32_e32 v26, 16, v168
	v_mul_f32_e32 v168, 0xbfb8aa3b, v26
	v_exp_f32_e32 v168, v168
	v_exp_f32_e32 v185, v184
	v_mul_f32_e32 v191, 0x45800000, v190
	v_add_f32_e32 v168, 1.0, v168
	v_rcp_f32_e32 v184, v168
	v_add_f32_e32 v168, 1.0, v185
	v_rcp_f32_e32 v185, v168
	v_cndmask_b32_e32 v168, v190, v191, vcc
	v_pk_mul_f32 v[190:191], v[204:205], v[168:169] op_sel_hi:[1,0]
	v_pk_mul_f32 v[26:27], v[184:185], v[26:27]
	v_lshlrev_b32_e32 v184, 16, v169
	v_mul_f32_e32 v185, 0xbfb8aa3b, v184
	s_waitcnt vmcnt(42)
	v_pk_mul_f32 v[28:29], v[28:29], v[190:191]
	v_exp_f32_e32 v190, v185
	v_and_b32_e32 v185, 0xffff0000, v169
	v_pk_mul_f32 v[26:27], v[26:27], v[28:29]
	v_mul_f32_e32 v28, 0xbfb8aa3b, v185
	v_exp_f32_e32 v29, v28
	v_cvt_pk_bf16_f32 v26, v26, v27
	v_add_f32_e32 v27, 1.0, v190
	v_pk_mul_f32 v[168:169], v[202:203], v[168:169] op_sel_hi:[1,0]
	v_rcp_f32_e32 v28, v27
	v_pk_mul_f32 v[30:31], v[30:31], v[168:169]
	v_add_f32_e32 v27, 1.0, v29
	v_lshlrev_b32_e32 v168, 16, v162
	v_rcp_f32_e32 v29, v27
	v_and_b32_e32 v169, 0xffff0000, v162
	v_mul_f32_e32 v27, 0xbfb8aa3b, v168
	v_exp_f32_e32 v27, v27
	v_mul_f32_e32 v162, 0xbfb8aa3b, v169
	v_exp_f32_e32 v190, v162
	v_pk_mul_f32 v[28:29], v[28:29], v[184:185]
	v_lshlrev_b32_e32 v184, 16, v163
	v_add_f32_e32 v27, 1.0, v27
	v_and_b32_e32 v185, 0xffff0000, v163
	v_mul_f32_e32 v163, 0xbfb8aa3b, v184
	v_rcp_f32_e32 v162, v27
	v_add_f32_e32 v27, 1.0, v190
	v_exp_f32_e32 v190, v163
	v_mul_f32_e32 v163, 0xbfb8aa3b, v185
	v_exp_f32_e32 v191, v163
	v_rcp_f32_e32 v163, v27
	v_add_f32_e32 v27, 1.0, v190
	v_rcp_f32_e32 v190, v27
	v_add_f32_e32 v27, 1.0, v191
	v_rcp_f32_e32 v191, v27
	v_pk_mul_f32 v[28:29], v[28:29], v[30:31]
	v_pk_mul_f32 v[30:31], v[162:163], v[168:169]
	v_lshlrev_b32_e32 v168, 16, v158
	v_pk_mul_f32 v[162:163], v[190:191], v[184:185]
	v_lshlrev_b32_e32 v184, 16, v156
	v_and_b32_e32 v185, 0xffff0000, v156
	v_mul_f32_e32 v156, 0x3d372713, v184
	v_and_b32_e32 v169, 0xffff0000, v158
	v_mul_f32_e32 v156, v156, v184
	v_mov_b32_e32 v158, v184
	v_fmac_f32_e32 v158, v156, v158
	v_mul_f32_e32 v156, 0x3f4c422a, v158
	v_mul_f32_e32 v158, 0x3d372713, v185
	v_mul_f32_e32 v158, v158, v185
	v_mov_b32_e32 v190, v185
	v_fmac_f32_e32 v190, v158, v190
	v_add_f32_e32 v156, v156, v156
	v_mul_f32_e32 v158, 0x3f4c422a, v190
	v_mul_f32_e32 v156, 0x3fb8aa3b, v156
	v_add_f32_e32 v158, v158, v158
	v_exp_f32_e32 v156, v156
	v_mul_f32_e32 v158, 0x3fb8aa3b, v158
	v_exp_f32_e32 v191, v158
	v_cvt_pk_bf16_f32 v27, v28, v29
	v_add_f32_e32 v156, 1.0, v156
	v_rcp_f32_e32 v190, v156
	v_add_f32_e32 v156, 1.0, v191
	v_lshlrev_b32_e32 v28, 16, v160
	v_and_b32_e32 v29, 0xffff0000, v160
	v_rcp_f32_e32 v191, v156
	v_lshlrev_b32_e32 v156, 16, v157
	v_pk_add_f32 v[28:29], v[168:169], v[28:29]
	v_pk_mul_f32 v[168:169], v[184:185], 0.5 op_sel_hi:[1,0]
	v_mul_f32_e32 v184, 0x3d372713, v156
	v_mul_f32_e32 v184, v184, v156
	v_mov_b32_e32 v185, v156
	v_and_b32_e32 v157, 0xffff0000, v157
	v_fmac_f32_e32 v185, v184, v185
	v_lshlrev_b32_e32 v160, 16, v161
	v_and_b32_e32 v161, 0xffff0000, v161
	v_lshlrev_b32_e32 v158, 16, v159
	v_and_b32_e32 v159, 0xffff0000, v159
	v_mul_f32_e32 v184, 0x3f4c422a, v185
	v_mul_f32_e32 v185, 0x3d372713, v157
	v_pk_add_f32 v[158:159], v[158:159], v[160:161]
	v_pk_fma_f32 v[160:161], v[190:191], 2.0, 1.0 op_sel_hi:[1,0,0] neg_lo:[1,0,0] neg_hi:[1,0,0]
	v_mul_f32_e32 v185, v185, v157
	v_mov_b32_e32 v190, v157
	v_fmac_f32_e32 v190, v185, v190
	v_mul_f32_e32 v185, 0x3f4c422a, v190
	v_add_f32_e32 v184, v184, v184
	v_add_f32_e32 v185, v185, v185
	v_mul_f32_e32 v184, 0x3fb8aa3b, v184
	v_mul_f32_e32 v185, 0x3fb8aa3b, v185
	v_exp_f32_e32 v184, v184
	v_exp_f32_e32 v185, v185
	v_pk_add_f32 v[160:161], v[160:161], 1.0 op_sel_hi:[1,0]
	v_pk_mul_f32 v[156:157], v[156:157], 0.5 op_sel_hi:[1,0]
	v_add_f32_e32 v184, 1.0, v184
	v_add_f32_e32 v185, 1.0, v185
	v_rcp_f32_e32 v184, v184
	v_rcp_f32_e32 v185, v185
	v_pk_mul_f32 v[160:161], v[168:169], v[160:161]
	s_waitcnt lgkmcnt(4)
	v_pk_add_f32 v[168:169], v[218:219], v[220:221]
	v_pk_mul_f32 v[28:29], v[28:29], v[160:161]
	v_pk_fma_f32 v[168:169], v[168:169], s[10:11], v[176:177] op_sel_hi:[1,0,0]
	v_cvt_pk_bf16_f32 v28, v28, v29
	v_mul_f32_e32 v29, 0x4b800000, v169
	v_cmp_gt_f32_e32 vcc, s7, v169
	v_pk_fma_f32 v[160:161], v[184:185], 2.0, 1.0 op_sel_hi:[1,0,0] neg_lo:[1,0,0] neg_hi:[1,0,0]
	v_cndmask_b32_e32 v29, v169, v29, vcc
	v_rsq_f32_e32 v169, v29
	v_pk_add_f32 v[160:161], v[160:161], 1.0 op_sel_hi:[1,0]
	v_pk_mul_f32 v[156:157], v[156:157], v[160:161]
	v_pk_mul_f32 v[156:157], v[158:159], v[156:157]
	s_nop 0
	v_cvt_pk_bf16_f32 v29, v156, v157
	v_mul_f32_e32 v156, 0x45800000, v169
	v_cndmask_b32_e32 v156, v169, v156, vcc
	v_pk_mul_f32 v[158:159], v[200:201], v[156:157] op_sel_hi:[1,0]
	v_cmp_gt_f32_e32 vcc, s7, v168
	s_waitcnt vmcnt(41)
	v_pk_mul_f32 v[20:21], v[20:21], v[158:159]
	v_pk_mul_f32 v[20:21], v[30:31], v[20:21]
	v_pk_mul_f32 v[30:31], v[198:199], v[156:157] op_sel_hi:[1,0]
	v_cvt_pk_bf16_f32 v20, v20, v21
	v_pk_mul_f32 v[22:23], v[22:23], v[30:31]
	s_nop 0
	v_pk_mul_f32 v[22:23], v[162:163], v[22:23]
	v_cvt_pk_bf16_f32 v21, v22, v23
	v_mul_f32_e32 v22, 0x4b800000, v168
	v_cndmask_b32_e32 v22, v168, v22, vcc
	v_rsq_f32_e32 v156, v22
	v_lshlrev_b32_e32 v22, 16, v154
	v_and_b32_e32 v23, 0xffff0000, v154
	v_mul_f32_e32 v30, 0xbfb8aa3b, v22
	v_mul_f32_e32 v31, 0xbfb8aa3b, v23
	v_exp_f32_e32 v30, v30
	v_exp_f32_e32 v31, v31
	v_mul_f32_e32 v154, 0x45800000, v156
	v_cndmask_b32_e32 v154, v156, v154, vcc
	v_add_f32_e32 v30, 1.0, v30
	v_add_f32_e32 v31, 1.0, v31
	v_rcp_f32_e32 v30, v30
	v_rcp_f32_e32 v31, v31
	v_pk_mul_f32 v[156:157], v[192:193], v[154:155] op_sel_hi:[1,0]
	s_waitcnt vmcnt(40)
	v_pk_mul_f32 v[16:17], v[16:17], v[156:157]
	v_pk_mul_f32 v[22:23], v[30:31], v[22:23]
	v_lshlrev_b32_e32 v30, 16, v155
	v_mul_f32_e32 v31, 0xbfb8aa3b, v30
	v_exp_f32_e32 v156, v31
	v_and_b32_e32 v31, 0xffff0000, v155
	v_pk_mul_f32 v[16:17], v[22:23], v[16:17]
	v_mul_f32_e32 v22, 0xbfb8aa3b, v31
	v_exp_f32_e32 v23, v22
	v_cvt_pk_bf16_f32 v16, v16, v17
	v_add_f32_e32 v17, 1.0, v156
	v_pk_mul_f32 v[154:155], v[182:183], v[154:155] op_sel_hi:[1,0]
	v_rcp_f32_e32 v22, v17
	v_pk_mul_f32 v[18:19], v[18:19], v[154:155]
	v_add_f32_e32 v17, 1.0, v23
	v_lshlrev_b32_e32 v154, 16, v152
	v_rcp_f32_e32 v23, v17
	v_and_b32_e32 v155, 0xffff0000, v152
	v_mul_f32_e32 v17, 0xbfb8aa3b, v154
	v_exp_f32_e32 v17, v17
	v_mul_f32_e32 v152, 0xbfb8aa3b, v155
	v_exp_f32_e32 v152, v152
	v_pk_mul_f32 v[22:23], v[22:23], v[30:31]
	v_add_f32_e32 v17, 1.0, v17
	v_rcp_f32_e32 v30, v17
	v_add_f32_e32 v17, 1.0, v152
	v_lshlrev_b32_e32 v152, 16, v153
	v_and_b32_e32 v153, 0xffff0000, v153
	v_mul_f32_e32 v31, 0xbfb8aa3b, v152
	v_exp_f32_e32 v156, v31
	v_mul_f32_e32 v31, 0xbfb8aa3b, v153
	v_exp_f32_e32 v157, v31
	v_rcp_f32_e32 v31, v17
	v_add_f32_e32 v17, 1.0, v156
	v_rcp_f32_e32 v156, v17
	v_add_f32_e32 v17, 1.0, v157
	v_rcp_f32_e32 v157, v17
	v_pk_mul_f32 v[18:19], v[22:23], v[18:19]
	v_pk_mul_f32 v[22:23], v[30:31], v[154:155]
	v_lshlrev_b32_e32 v154, 16, v146
	v_and_b32_e32 v155, 0xffff0000, v146
	v_mul_f32_e32 v146, 0x3d372713, v154
	v_pk_mul_f32 v[30:31], v[156:157], v[152:153]
	v_lshlrev_b32_e32 v152, 16, v148
	v_and_b32_e32 v153, 0xffff0000, v148
	v_mul_f32_e32 v146, v146, v154
	v_mov_b32_e32 v148, v154
	v_fmac_f32_e32 v148, v146, v148
	v_mul_f32_e32 v146, 0x3f4c422a, v148
	v_mul_f32_e32 v148, 0x3d372713, v155
	v_mul_f32_e32 v148, v148, v155
	v_mov_b32_e32 v156, v155
	v_fmac_f32_e32 v156, v148, v156
	v_add_f32_e32 v146, v146, v146
	v_mul_f32_e32 v148, 0x3f4c422a, v156
	v_mul_f32_e32 v146, 0x3fb8aa3b, v146
	v_add_f32_e32 v148, v148, v148
	v_exp_f32_e32 v146, v146
	v_mul_f32_e32 v148, 0x3fb8aa3b, v148
	v_exp_f32_e32 v157, v148
	v_cvt_pk_bf16_f32 v17, v18, v19
	v_add_f32_e32 v146, 1.0, v146
	v_rcp_f32_e32 v156, v146
	v_add_f32_e32 v146, 1.0, v157
	v_lshlrev_b32_e32 v18, 16, v150
	v_and_b32_e32 v19, 0xffff0000, v150
	v_rcp_f32_e32 v157, v146
	v_lshlrev_b32_e32 v146, 16, v147
	v_pk_add_f32 v[18:19], v[152:153], v[18:19]
	v_pk_mul_f32 v[152:153], v[154:155], 0.5 op_sel_hi:[1,0]
	v_mul_f32_e32 v154, 0x3d372713, v146
	v_mul_f32_e32 v154, v154, v146
	v_mov_b32_e32 v155, v146
	v_and_b32_e32 v147, 0xffff0000, v147
	v_fmac_f32_e32 v155, v154, v155
	v_lshlrev_b32_e32 v150, 16, v151
	v_and_b32_e32 v151, 0xffff0000, v151
	v_lshlrev_b32_e32 v148, 16, v149
	v_and_b32_e32 v149, 0xffff0000, v149
	v_mul_f32_e32 v154, 0x3f4c422a, v155
	v_mul_f32_e32 v155, 0x3d372713, v147
	v_pk_add_f32 v[148:149], v[148:149], v[150:151]
	v_pk_fma_f32 v[150:151], v[156:157], 2.0, 1.0 op_sel_hi:[1,0,0] neg_lo:[1,0,0] neg_hi:[1,0,0]
	v_mul_f32_e32 v155, v155, v147
	v_mov_b32_e32 v156, v147
	v_fmac_f32_e32 v156, v155, v156
	v_mul_f32_e32 v155, 0x3f4c422a, v156
	v_add_f32_e32 v154, v154, v154
	v_add_f32_e32 v155, v155, v155
	v_mul_f32_e32 v154, 0x3fb8aa3b, v154
	v_mul_f32_e32 v155, 0x3fb8aa3b, v155
	v_exp_f32_e32 v154, v154
	v_exp_f32_e32 v155, v155
	v_pk_add_f32 v[150:151], v[150:151], 1.0 op_sel_hi:[1,0]
	v_pk_mul_f32 v[146:147], v[146:147], 0.5 op_sel_hi:[1,0]
	v_add_f32_e32 v154, 1.0, v154
	v_add_f32_e32 v155, 1.0, v155
	v_rcp_f32_e32 v154, v154
	v_rcp_f32_e32 v155, v155
	v_pk_mul_f32 v[150:151], v[152:153], v[150:151]
	s_waitcnt lgkmcnt(2)
	v_pk_add_f32 v[152:153], v[210:211], v[212:213]
	v_pk_mul_f32 v[18:19], v[18:19], v[150:151]
	v_pk_fma_f32 v[152:153], v[152:153], s[10:11], v[176:177] op_sel_hi:[1,0,0]
	v_cvt_pk_bf16_f32 v18, v18, v19
	v_mul_f32_e32 v19, 0x4b800000, v153
	v_cmp_gt_f32_e32 vcc, s7, v153
	v_pk_fma_f32 v[150:151], v[154:155], 2.0, 1.0 op_sel_hi:[1,0,0] neg_lo:[1,0,0] neg_hi:[1,0,0]
	v_cndmask_b32_e32 v19, v153, v19, vcc
	v_rsq_f32_e32 v153, v19
	v_pk_add_f32 v[150:151], v[150:151], 1.0 op_sel_hi:[1,0]
	v_pk_mul_f32 v[146:147], v[146:147], v[150:151]
	v_pk_mul_f32 v[146:147], v[148:149], v[146:147]
	s_nop 0
	v_cvt_pk_bf16_f32 v19, v146, v147
	v_mul_f32_e32 v146, 0x45800000, v153
	v_cndmask_b32_e32 v146, v153, v146, vcc
	v_pk_mul_f32 v[148:149], v[188:189], v[146:147] op_sel_hi:[1,0]
	v_cmp_gt_f32_e32 vcc, s7, v152
	s_waitcnt vmcnt(39)
	v_pk_mul_f32 v[8:9], v[8:9], v[148:149]
	v_pk_mul_f32 v[8:9], v[22:23], v[8:9]
	v_pk_mul_f32 v[22:23], v[186:187], v[146:147] op_sel_hi:[1,0]
	v_cvt_pk_bf16_f32 v8, v8, v9
	v_pk_mul_f32 v[10:11], v[10:11], v[22:23]
	s_nop 0
	v_pk_mul_f32 v[10:11], v[30:31], v[10:11]
	s_nop 0
	v_cvt_pk_bf16_f32 v9, v10, v11
	v_mul_f32_e32 v10, 0x4b800000, v152
	v_cndmask_b32_e32 v10, v152, v10, vcc
	v_rsq_f32_e32 v30, v10
	v_lshlrev_b32_e32 v10, 16, v144
	v_and_b32_e32 v11, 0xffff0000, v144
	v_mul_f32_e32 v22, 0xbfb8aa3b, v10
	v_mul_f32_e32 v23, 0xbfb8aa3b, v11
	v_exp_f32_e32 v22, v22
	v_exp_f32_e32 v23, v23
	v_mul_f32_e32 v31, 0x45800000, v30
	v_cndmask_b32_e32 v30, v30, v31, vcc
	v_add_f32_e32 v22, 1.0, v22
	v_add_f32_e32 v23, 1.0, v23
	v_rcp_f32_e32 v22, v22
	v_rcp_f32_e32 v23, v23
	v_pk_mul_f32 v[146:147], v[172:173], v[30:31] op_sel_hi:[1,0]
	s_waitcnt vmcnt(38)
	v_pk_mul_f32 v[12:13], v[12:13], v[146:147]
	v_pk_mul_f32 v[10:11], v[22:23], v[10:11]
	v_lshlrev_b32_e32 v22, 16, v145
	v_mul_f32_e32 v23, 0xbfb8aa3b, v22
	v_exp_f32_e32 v31, v23
	v_and_b32_e32 v23, 0xffff0000, v145
	v_pk_mul_f32 v[10:11], v[10:11], v[12:13]
	v_mul_f32_e32 v12, 0xbfb8aa3b, v23
	v_exp_f32_e32 v13, v12
	v_cvt_pk_bf16_f32 v10, v10, v11
	v_add_f32_e32 v11, 1.0, v31
	v_pk_mul_f32 v[30:31], v[170:171], v[30:31] op_sel_hi:[1,0]
	v_rcp_f32_e32 v12, v11
	v_pk_mul_f32 v[14:15], v[14:15], v[30:31]
	v_add_f32_e32 v11, 1.0, v13
	v_lshlrev_b32_e32 v30, 16, v142
	v_rcp_f32_e32 v13, v11
	v_and_b32_e32 v31, 0xffff0000, v142
	v_mul_f32_e32 v11, 0xbfb8aa3b, v30
	v_exp_f32_e32 v11, v11
	v_mul_f32_e32 v142, 0xbfb8aa3b, v31
	v_exp_f32_e32 v142, v142
	v_pk_mul_f32 v[12:13], v[12:13], v[22:23]
	v_add_f32_e32 v11, 1.0, v11
	v_rcp_f32_e32 v22, v11
	v_add_f32_e32 v11, 1.0, v142
	v_lshlrev_b32_e32 v142, 16, v143
	v_and_b32_e32 v143, 0xffff0000, v143
	v_mul_f32_e32 v23, 0xbfb8aa3b, v142
	v_exp_f32_e32 v144, v23
	v_mul_f32_e32 v23, 0xbfb8aa3b, v143
	v_exp_f32_e32 v145, v23
	v_rcp_f32_e32 v23, v11
	v_add_f32_e32 v11, 1.0, v144
	v_rcp_f32_e32 v144, v11
	v_add_f32_e32 v11, 1.0, v145
	v_rcp_f32_e32 v145, v11
	v_pk_mul_f32 v[12:13], v[12:13], v[14:15]
	v_cvt_pk_bf16_f32 v11, v12, v13
	v_pk_mul_f32 v[14:15], v[144:145], v[142:143]
	v_lshlrev_b32_e32 v142, 16, v126
	v_and_b32_e32 v143, 0xffff0000, v126
	v_mul_f32_e32 v126, 0x3d372713, v142
	v_pk_mul_f32 v[12:13], v[22:23], v[30:31]
	v_lshlrev_b32_e32 v22, 16, v140
	v_and_b32_e32 v23, 0xffff0000, v140
	v_lshlrev_b32_e32 v30, 16, v141
	v_and_b32_e32 v31, 0xffff0000, v141
	v_lshlrev_b32_e32 v140, 16, v130
	v_and_b32_e32 v141, 0xffff0000, v130
	v_mul_f32_e32 v126, v126, v142
	v_mov_b32_e32 v130, v142
	v_fmac_f32_e32 v130, v126, v130
	v_mul_f32_e32 v126, 0x3f4c422a, v130
	v_mul_f32_e32 v130, 0x3d372713, v143
	v_mul_f32_e32 v130, v130, v143
	v_mov_b32_e32 v144, v143
	v_fmac_f32_e32 v144, v130, v144
	v_add_f32_e32 v126, v126, v126
	v_mul_f32_e32 v130, 0x3f4c422a, v144
	v_mul_f32_e32 v126, 0x3fb8aa3b, v126
	v_add_f32_e32 v130, v130, v130
	v_exp_f32_e32 v126, v126
	v_mul_f32_e32 v130, 0x3fb8aa3b, v130
	v_exp_f32_e32 v145, v130
	v_pk_add_f32 v[22:23], v[22:23], v[140:141]
	v_add_f32_e32 v126, 1.0, v126
	v_rcp_f32_e32 v144, v126
	v_add_f32_e32 v126, 1.0, v145
	v_rcp_f32_e32 v145, v126
	v_lshlrev_b32_e32 v126, 16, v127
	v_pk_mul_f32 v[140:141], v[142:143], 0.5 op_sel_hi:[1,0]
	v_mul_f32_e32 v142, 0x3d372713, v126
	v_mul_f32_e32 v142, v142, v126
	v_mov_b32_e32 v143, v126
	v_and_b32_e32 v127, 0xffff0000, v127
	v_fmac_f32_e32 v143, v142, v143
	v_lshlrev_b32_e32 v130, 16, v131
	v_and_b32_e32 v131, 0xffff0000, v131
	v_mul_f32_e32 v142, 0x3f4c422a, v143
	v_mul_f32_e32 v143, 0x3d372713, v127
	v_pk_add_f32 v[30:31], v[30:31], v[130:131]
	v_pk_fma_f32 v[130:131], v[144:145], 2.0, 1.0 op_sel_hi:[1,0,0] neg_lo:[1,0,0] neg_hi:[1,0,0]
	v_mul_f32_e32 v143, v143, v127
	v_mov_b32_e32 v144, v127
	v_fmac_f32_e32 v144, v143, v144
	v_mul_f32_e32 v143, 0x3f4c422a, v144
	v_add_f32_e32 v142, v142, v142
	v_add_f32_e32 v143, v143, v143
	v_mul_f32_e32 v142, 0x3fb8aa3b, v142
	v_mul_f32_e32 v143, 0x3fb8aa3b, v143
	v_exp_f32_e32 v142, v142
	v_exp_f32_e32 v143, v143
	v_pk_add_f32 v[130:131], v[130:131], 1.0 op_sel_hi:[1,0]
	v_pk_mul_f32 v[126:127], v[126:127], 0.5 op_sel_hi:[1,0]
	v_add_f32_e32 v142, 1.0, v142
	v_add_f32_e32 v143, 1.0, v143
	v_rcp_f32_e32 v142, v142
	v_rcp_f32_e32 v143, v143
	v_pk_mul_f32 v[130:131], v[140:141], v[130:131]
	s_waitcnt lgkmcnt(0)
	v_pk_add_f32 v[140:141], v[194:195], v[196:197]
	v_pk_mul_f32 v[22:23], v[22:23], v[130:131]
	v_pk_fma_f32 v[140:141], v[140:141], s[10:11], v[176:177] op_sel_hi:[1,0,0]
	v_cvt_pk_bf16_f32 v22, v22, v23
	v_mul_f32_e32 v23, 0x4b800000, v141
	v_cmp_gt_f32_e32 vcc, s7, v141
	v_pk_fma_f32 v[130:131], v[142:143], 2.0, 1.0 op_sel_hi:[1,0,0] neg_lo:[1,0,0] neg_hi:[1,0,0]
	v_cndmask_b32_e32 v23, v141, v23, vcc
	v_rsq_f32_e32 v141, v23
	v_pk_add_f32 v[130:131], v[130:131], 1.0 op_sel_hi:[1,0]
	v_pk_mul_f32 v[126:127], v[126:127], v[130:131]
	v_pk_mul_f32 v[30:31], v[30:31], v[126:127]
	v_cvt_pk_bf16_f32 v23, v30, v31
	v_mul_f32_e32 v30, 0x45800000, v141
	v_cndmask_b32_e32 v30, v141, v30, vcc
	v_pk_mul_f32 v[126:127], v[180:181], v[30:31] op_sel_hi:[1,0]
	v_cmp_gt_f32_e32 vcc, s7, v140
	s_waitcnt vmcnt(37)
	v_pk_mul_f32 v[0:1], v[0:1], v[126:127]
	v_pk_mul_f32 v[0:1], v[12:13], v[0:1]
	v_pk_mul_f32 v[12:13], v[178:179], v[30:31] op_sel_hi:[1,0]
	v_cvt_pk_bf16_f32 v0, v0, v1
	v_pk_mul_f32 v[2:3], v[2:3], v[12:13]
	s_nop 0
	v_pk_mul_f32 v[2:3], v[14:15], v[2:3]
	s_nop 0
	v_cvt_pk_bf16_f32 v1, v2, v3
	v_mul_f32_e32 v2, 0x4b800000, v140
	v_cndmask_b32_e32 v2, v140, v2, vcc
	v_rsq_f32_e32 v14, v2
	v_lshlrev_b32_e32 v2, 16, v94
	v_and_b32_e32 v3, 0xffff0000, v94
	v_mul_f32_e32 v12, 0xbfb8aa3b, v2
	v_mul_f32_e32 v13, 0xbfb8aa3b, v3
	v_exp_f32_e32 v12, v12
	v_exp_f32_e32 v13, v13
	v_mul_f32_e32 v15, 0x45800000, v14
	v_cndmask_b32_e32 v14, v14, v15, vcc
	v_add_f32_e32 v12, 1.0, v12
	v_add_f32_e32 v13, 1.0, v13
	v_rcp_f32_e32 v12, v12
	v_rcp_f32_e32 v13, v13
	v_pk_mul_f32 v[30:31], v[166:167], v[14:15] op_sel_hi:[1,0]
	s_waitcnt vmcnt(36)
	v_pk_mul_f32 v[4:5], v[4:5], v[30:31]
	v_pk_mul_f32 v[2:3], v[12:13], v[2:3]
	v_lshlrev_b32_e32 v12, 16, v95
	v_and_b32_e32 v13, 0xffff0000, v95
	v_mul_f32_e32 v15, 0xbfb8aa3b, v12
	v_mul_f32_e32 v30, 0xbfb8aa3b, v13
	v_exp_f32_e32 v15, v15
	v_exp_f32_e32 v30, v30
	v_pk_mul_f32 v[2:3], v[2:3], v[4:5]
	v_add_f32_e32 v4, 1.0, v15
	v_add_f32_e32 v5, 1.0, v30
	v_rcp_f32_e32 v4, v4
	v_rcp_f32_e32 v5, v5
	v_pk_mul_f32 v[14:15], v[164:165], v[14:15] op_sel_hi:[1,0]
	v_cvt_pk_bf16_f32 v2, v2, v3
	v_pk_mul_f32 v[6:7], v[6:7], v[14:15]
	v_pk_mul_f32 v[4:5], v[4:5], v[12:13]
	s_nop 0
	v_pk_mul_f32 v[4:5], v[4:5], v[6:7]
	s_nop 0
	v_cvt_pk_bf16_f32 v3, v4, v5
	v_add_co_u32_e32 v4, vcc, s11, v84
	s_nop 1
	v_addc_co_u32_e32 v5, vcc, -1, v85, vcc
	v_add_co_u32_e32 v6, vcc, s13, v84
	global_store_dwordx2 v[4:5], v[24:25], off offset:-1536
	s_nop 0
	v_addc_co_u32_e32 v7, vcc, -1, v85, vcc
	global_store_dwordx2 v[6:7], v[174:175], off offset:-1536
	global_store_dwordx2 v[84:85], v[26:27], off offset:-1536
	global_store_dwordx2 v[4:5], v[20:21], off offset:-1024
	global_store_dwordx2 v[6:7], v[28:29], off offset:-1024
	global_store_dwordx2 v[84:85], v[16:17], off offset:-1024
	global_store_dwordx2 v[4:5], v[8:9], off offset:-512
	global_store_dwordx2 v[6:7], v[18:19], off offset:-512
	global_store_dwordx2 v[84:85], v[10:11], off offset:-512
	global_store_dwordx2 v[4:5], v[0:1], off
	global_store_dwordx2 v[6:7], v[22:23], off
	global_store_dwordx2 v[84:85], v[2:3], off
	v_lshl_add_u64 v[84:85], v[84:85], 0, s[8:9]
	s_andn2_b64 vcc, exec, s[14:15]
	s_waitcnt vmcnt(12)
	v_mov_b64_e32 v[184:185], v[100:101]
	v_mov_b64_e32 v[190:191], v[102:103]
	v_mov_b64_e32 v[160:161], v[116:117]
	v_mov_b64_e32 v[158:159], v[120:121]
	v_mov_b64_e32 v[162:163], v[124:125]
	v_mov_b64_e32 v[168:169], v[98:99]
	v_mov_b64_e32 v[154:155], v[106:107]
	v_mov_b64_e32 v[156:157], v[104:105]
	v_mov_b64_e32 v[150:151], v[112:113]
	v_mov_b64_e32 v[148:149], v[114:115]
	v_mov_b64_e32 v[152:153], v[110:111]
	v_mov_b64_e32 v[146:147], v[108:109]
	v_mov_b64_e32 v[176:177], v[118:119]
	v_mov_b64_e32 v[144:145], v[132:133]
	v_mov_b64_e32 v[142:143], v[134:135]
	v_mov_b64_e32 v[130:131], v[128:129]
	v_mov_b64_e32 v[126:127], v[136:137]
	v_mov_b64_e32 v[140:141], v[122:123]
	v_mov_b64_e32 v[94:95], v[138:139]
	v_mov_b64_e32 v[174:175], v[96:97]
	s_cbranch_vccz .LBB0_2537
